# adds to the previous version: attention K tile LDS swizzle gets a fourth XOR bit ((row>>4)&1)<<7 on write and read so ds_read_b128 lane groups cover all 64 banks
# speedup vs baseline: 1.0092x; 1.0092x over previous
.LBB0_783:
	s_and_b64 vcc, exec, s[0:1]
	s_cbranch_vccz .LBB0_762
	s_ashr_i32 s0, s16, 7
	s_lshl_b32 s18, s0, 11
	s_and_b32 s1, s17, 0x780
	s_or_b32 s17, s18, s1
	s_lshl_b32 s1, s16, 3
	s_and_b32 s1, s1, 0x380
	v_mbcnt_lo_u32_b32 v171, -1, 0
	v_mbcnt_hi_u32_b32 v171, -1, v171
	s_lshl_b32 s96, s1, 1
	v_lshlrev_b32_e32 v20, 3, v171
	v_and_b32_e32 v0, 0x78, v20
	s_add_u32 s20, s6, s96
	v_lshlrev_b32_e32 v16, 1, v0
	s_addc_u32 s21, s7, 0
	v_mov_b32_e32 v17, v113
	v_add_u32_e32 v172, s4, v171
	v_lshl_add_u64 v[166:167], s[20:21], 0, v[16:17]
	s_add_u32 s20, s8, s96
	v_ashrrev_i32_e32 v181, 4, v172
	s_addc_u32 s21, s9, 0
	v_lshl_add_u64 v[168:169], s[20:21], 0, v[16:17]
	v_add_u32_e32 v34, s18, v181
	v_mad_i64_i32 v[0:1], s[20:21], v34, s62, v[168:169]
	v_add_co_u32_e32 v4, vcc, s74, v0
	v_mad_i64_i32 v[8:9], s[20:21], v34, s62, v[166:167]
	s_nop 0
	v_addc_co_u32_e32 v5, vcc, 0, v1, vcc
	v_add_co_u32_e32 v12, vcc, s74, v8
	global_load_dwordx4 v[0:3], v[0:1], off
	s_nop 0
	global_load_dwordx4 v[4:7], v[4:5], off
	v_addc_co_u32_e32 v13, vcc, 0, v9, vcc
	global_load_dwordx4 v[8:11], v[8:9], off
	s_nop 0
	global_load_dwordx4 v[12:15], v[12:13], off
	v_lshrrev_b32_e32 v17, 1, v172
	v_and_b32_e32 v173, 31, v171
	v_and_b32_e32 v176, 0x60, v17
	v_mov_b64_e32 v[18:19], s[50:51]
	v_ashrrev_i32_e32 v175, 8, v172
	v_or3_b32 v29, v173, s17, v176
	v_bfe_u32 v22, v20, 5, 2
	v_lshlrev_b32_e32 v20, 6, v175
	v_mad_i64_i32 v[18:19], s[20:21], v29, s62, v[18:19]
	v_bfe_u32 v174, v171, 5, 1
	v_ashrrev_i32_e32 v21, 31, v20
	v_lshl_add_u64 v[18:19], v[18:19], 0, s[96:97]
	v_lshlrev_b32_e32 v112, 4, v174
	v_lshl_add_u64 v[18:19], v[20:21], 1, v[18:19]
	v_lshl_add_u64 v[18:19], v[18:19], 0, v[112:113]
	global_load_dwordx4 v[122:125], v[18:19], off
	global_load_dwordx4 v[126:129], v[18:19], off offset:32
	global_load_dwordx4 v[118:121], v[18:19], off offset:64
	global_load_dwordx4 v[114:117], v[18:19], off offset:96
	v_and_b32_e32 v17, 0xfffff0, v181
	v_lshlrev_b32_e32 v24, 1, v181
	v_add_u32_e32 v27, 32, v181
	v_lshrrev_b32_e32 v25, 1, v181
	v_and_b32_e32 v26, 3, v181
	v_and_or_b32 v17, v24, 8, v17
	v_and_b32_e32 v20, 0xfffff0, v27
	v_lshlrev_b32_e32 v21, 1, v27
	v_and_b32_e32 v23, 0x70, v172
	v_lshlrev_b32_e32 v28, 8, v181
	v_and_or_b32 v24, v25, 4, v26
	v_lshlrev_b32_e32 v26, 8, v27
	v_lshrrev_b32_e32 v17, 1, v17
	v_and_or_b32 v20, v21, 8, v20
	v_and_b32_e32 v25, 48, v16
	v_bitop3_b32 v182, v16, v28, v23 bitop3:0xde
	v_bitop3_b32 v183, v26, v16, v23 bitop3:0xf6
	v_and_b32_e32 v243, 16, v181
	v_lshlrev_b32_e32 v243, 3, v243
	v_xor_b32_e32 v182, v243, v182
	v_xor_b32_e32 v183, v243, v183
	v_or_b32_e32 v16, v17, v22
	v_lshrrev_b32_e32 v17, 1, v20
	v_lshlrev_b32_e32 v24, 6, v24
	v_lshlrev_b32_e32 v16, 9, v16
	v_or_b32_e32 v17, v17, v22
	v_or3_b32 v184, v16, v24, v25
	v_lshlrev_b32_e32 v16, 9, v17
	v_or3_b32 v185, v16, v24, v25
	v_add_u32_e32 v32, 0, v184
	v_add_u32_e32 v21, 0, v182
	v_add_u32_e32 v20, 0, v183
	v_add_u32_e32 v33, 0, v185
	s_waitcnt vmcnt(0)
	v_lshlrev_b32_e32 v38, 7, v175
	v_lshlrev_b32_e32 v189, 8, v173
	v_add_u32_e32 v191, 0, v189
	s_movk_i32 s1, 0x60
	s_waitcnt vmcnt(7)
	ds_write_b128 v32, v[0:3] offset:1024
	s_waitcnt vmcnt(6)
	ds_write_b128 v33, v[4:7] offset:1024
	s_waitcnt vmcnt(5)
	ds_write_b128 v21, v[8:11] offset:50176
	s_waitcnt vmcnt(4)
	ds_write_b128 v20, v[12:15] offset:50176
	v_add_u32_e32 v4, 64, v34
	v_mad_i64_i32 v[0:1], s[20:21], v4, s62, v[168:169]
	v_add_co_u32_e32 v2, vcc, s74, v0
	s_nop 1
	v_addc_co_u32_e32 v3, vcc, 0, v1, vcc
	global_load_dwordx4 v[16:19], v[0:1], off
	global_load_dwordx4 v[20:23], v[2:3], off
	v_mad_i64_i32 v[0:1], s[20:21], v4, s62, v[166:167]
	v_add_co_u32_e32 v2, vcc, s74, v0
	v_add_u32_e32 v4, 0x80, v34
	s_nop 0
	v_addc_co_u32_e32 v3, vcc, 0, v1, vcc
	global_load_dwordx4 v[24:27], v[0:1], off
	global_load_dwordx4 v[28:31], v[2:3], off
	v_mad_i64_i32 v[0:1], s[20:21], v4, s62, v[166:167]
	v_add_co_u32_e32 v2, vcc, s74, v0
	s_nop 1
	v_addc_co_u32_e32 v3, vcc, 0, v1, vcc
	global_load_dwordx4 v[142:145], v[2:3], off
	global_load_dwordx4 v[138:141], v[0:1], off
	v_mad_i64_i32 v[0:1], s[20:21], v4, s62, v[168:169]
	v_add_co_u32_e32 v2, vcc, s74, v0
	s_nop 1
	v_addc_co_u32_e32 v3, vcc, 0, v1, vcc
	global_load_dwordx4 v[134:137], v[2:3], off
	global_load_dwordx4 v[130:133], v[0:1], off
	v_lshlrev_b32_e32 v0, 4, v171
	v_and_b32_e32 v39, 0x70, v0
	v_bitop3_b32 v190, v38, v39, v112 bitop3:0x36
	v_and_b32_e32 v244, 16, v171
	v_lshlrev_b32_e32 v244, 3, v244
	v_xor_b32_e32 v190, v244, v190
	v_add_u32_e32 v34, v191, v190
	s_waitcnt lgkmcnt(0)
	s_barrier
	ds_read_b128 v[0:3], v34 offset:50176
	ds_read_b128 v[34:37], v34 offset:58368
	v_or_b32_e32 v38, v38, v112
	v_bitop3_b32 v188, v38, v39, 32 bitop3:0x36
	v_xor_b32_e32 v188, v244, v188
	v_add_u32_e32 v40, v191, v188
	s_waitcnt vmcnt(11) lgkmcnt(0)
	v_mfma_f32_32x32x16_bf16 v[64:79], v[34:37], v[122:125], 0
	ds_read_b128 v[34:37], v40 offset:50176
	v_bitop3_b32 v187, v38, v39, 64 bitop3:0x36
	v_bitop3_b32 v186, v38, v39, s1 bitop3:0x36
	v_xor_b32_e32 v187, v244, v187
	v_xor_b32_e32 v186, v244, v186
	v_add_u32_e32 v38, v191, v186
	v_mfma_f32_32x32x16_bf16 v[0:15], v[0:3], v[122:125], 0
	s_waitcnt vmcnt(10) lgkmcnt(0)
	v_mfma_f32_32x32x16_bf16 v[0:15], v[34:37], v[126:129], v[0:15]
	ds_read_b128 v[34:37], v40 offset:58368
	v_add_u32_e32 v40, v191, v187
	s_waitcnt lgkmcnt(0)
	v_mfma_f32_32x32x16_bf16 v[64:79], v[34:37], v[126:129], v[64:79]
	ds_read_b128 v[34:37], v40 offset:50176
	s_waitcnt vmcnt(9) lgkmcnt(0)
	v_mfma_f32_32x32x16_bf16 v[0:15], v[34:37], v[118:121], v[0:15]
	ds_read_b128 v[34:37], v40 offset:58368
	s_waitcnt lgkmcnt(0)
	v_mfma_f32_32x32x16_bf16 v[64:79], v[34:37], v[118:121], v[64:79]
	ds_read_b128 v[34:37], v38 offset:50176
	s_waitcnt vmcnt(8) lgkmcnt(0)
	v_mfma_f32_32x32x16_bf16 v[0:15], v[34:37], v[114:117], v[0:15]
	ds_read_b128 v[34:37], v38 offset:58368
	s_waitcnt lgkmcnt(0)
	v_mfma_f32_32x32x16_bf16 v[64:79], v[34:37], v[114:117], v[64:79]
	s_nop 8
	v_max_f32_e32 v34, v1, v1
	v_max_f32_e32 v35, v0, v0
	v_max_f32_e32 v34, v35, v34
	v_max3_f32 v34, v34, v2, v3
	v_max3_f32 v34, v34, v4, v5
	v_max3_f32 v34, v34, v6, v7
	v_max3_f32 v34, v34, v8, v9
	v_max3_f32 v34, v34, v10, v11
	v_max3_f32 v34, v34, v12, v13
	v_max3_f32 v34, v34, v14, v15
	v_max3_f32 v34, v34, v64, v65
	v_max3_f32 v34, v34, v66, v67
	v_max3_f32 v34, v34, v68, v69
	v_max3_f32 v34, v34, v70, v71
	v_max3_f32 v34, v34, v72, v73
	v_max3_f32 v34, v34, v74, v75
	v_max3_f32 v34, v34, v76, v77
	v_max3_f32 v34, v34, v78, v79
	v_mov_b32_e32 v35, v34
	s_nop 1
	v_permlane32_swap_b32_e32 v34, v35
	v_max_f32_e32 v35, v35, v35
	v_max_f32_e32 v34, v34, v34
	v_max_f32_e32 v34, v34, v35
	v_cmp_ge_f32_e32 vcc, s75, v34
	s_cmp_eq_u64 vcc, exec
	s_cbranch_scc0 .LBB0_814
	v_mov_b32_e32 v193, 1.0
	v_mov_b32_e32 v164, 0
